# speedup vs baseline: 1.0473x; 1.0473x over previous
_Z14k1_stats_graphPKfS0_S0_PdPfPiPyPtS2_S3_:
	s_load_dwordx4 s[4:7], s[0:1], 0x0
	s_load_dwordx4 s[12:15], s[0:1], 0x30
	s_and_b32 s3, s2, 7
	s_lshr_b32 s2, s2, 3
	s_lshl_b32 s3, s3, 8
	s_add_u32 s2, s2, s3
	v_and_b32_e32 v1, 63, v0
	v_lshrrev_b32_e32 v2, 6, v0
	v_lshlrev_b32_e32 v12, 4, v1
	v_add_u32_e32 v13, 0x1000, v12
	v_mov_b32_e32 v15, 0xff800000
	v_readfirstlane_b32 s3, v2
	s_lshl_b32 s24, s2, 2
	s_add_u32 s24, s24, s3
	s_lshr_b32 s25, s24, 9
	s_and_b32 s26, s24, 0x1ff
	s_lshl_b32 s27, s24, 4
	s_lshl_b32 s32, s25, 9
	s_lshl_b32 s33, s3, 7
	s_add_u32 s32, s32, s33
	v_add_u32_e32 v3, s32, v1
	v_lshlrev_b32_e32 v3, 4, v3
	s_mul_i32 s34, s24, 0x641
	s_and_b32 s35, s34, 3
	s_andn2_b32 s34, s34, 3
	s_lshl_b32 s34, s34, 2
	s_waitcnt lgkmcnt(0)
	s_load_dwordx4 s[28:31], s[4:5], s27
	global_load_dwordx4 v[4:7], v3, s[4:5]
	global_load_dwordx4 v[8:11], v3, s[4:5] offset:1024
	s_add_u32 s36, s6, s34
	s_addc_u32 s37, s7, 0
	global_load_dwordx4 v[16:19], v12, s[36:37] offset:0 nt
	global_load_dwordx4 v[20:23], v12, s[36:37] offset:1024 nt
	global_load_dwordx4 v[24:27], v12, s[36:37] offset:2048 nt
	global_load_dwordx4 v[28:31], v12, s[36:37] offset:3072 nt
	global_load_dwordx4 v[32:35], v13, s[36:37] offset:0 nt
	global_load_dwordx4 v[36:39], v13, s[36:37] offset:1024 nt
	v_mov_b32_e32 v40, v15
	v_mov_b32_e32 v41, v15
	v_mov_b32_e32 v42, v15
	v_mov_b32_e32 v43, v15
	s_mov_b64 exec, 0x1ffff
	global_load_dwordx4 v[40:43], v13, s[36:37] offset:2048 nt
	s_mov_b64 exec, -1
	s_lshl_b32 s33, s3, 11
	v_add_u32_e32 v14, s33, v12
	s_mov_b32 s39, 0xb8d1b717
	v_mov_b32_e32 v60, 0x7f800000
	s_waitcnt vmcnt(7)
	ds_write_b128 v14, v[4:7]
	ds_write_b128 v14, v[8:11] offset:1024
	s_waitcnt lgkmcnt(0)
	v_mov_b32_e32 v52, s28
	v_mov_b32_e32 v53, s29
	v_sub_f32_e32 v52, s30, v52
	v_sub_f32_e32 v53, s31, v53
	v_mul_f32_e32 v52, v52, v53
	s_barrier
	v_readfirstlane_b32 s38, v52
	ds_read_b128 v[4:7], v12 offset:0
	ds_read_b128 v[8:11], v12 offset:1024
	ds_read_b128 v[44:47], v12 offset:2048
	ds_read_b128 v[48:51], v12 offset:3072
	s_waitcnt lgkmcnt(3)
	v_sub_f32_e32 v52, v6, v4
	v_sub_f32_e32 v53, v7, v5
	v_min_f32_e32 v54, s30, v6
	v_max_f32_e32 v55, s28, v4
	v_min_f32_e32 v56, s31, v7
	v_max_f32_e32 v57, s29, v5
	v_mul_f32_e32 v52, v52, v53
	v_sub_f32_e32 v54, v54, v55
	v_sub_f32_e32 v56, v56, v57
	v_max_f32_e32 v54, 0, v54
	v_max_f32_e32 v56, 0, v56
	v_add_f32_e32 v52, s38, v52
	v_mul_f32_e32 v54, v54, v56
	v_sub_f32_e32 v52, v52, v54
	v_fma_f32 v55, v52, -0.5, v54
	v_fma_f32 v53, v52, s39, |v55|
	v_cmp_gt_f32_e64 s[40:41], v55, 0
	v_min_f32_e32 v60, v60, v53
	ds_read_b128 v[4:7], v12 offset:4096
	s_waitcnt lgkmcnt(3)
	v_sub_f32_e32 v52, v10, v8
	v_sub_f32_e32 v53, v11, v9
	v_min_f32_e32 v54, s30, v10
	v_max_f32_e32 v55, s28, v8
	v_min_f32_e32 v56, s31, v11
	v_max_f32_e32 v57, s29, v9
	v_mul_f32_e32 v52, v52, v53
	v_sub_f32_e32 v54, v54, v55
	v_sub_f32_e32 v56, v56, v57
	v_max_f32_e32 v54, 0, v54
	v_max_f32_e32 v56, 0, v56
	v_add_f32_e32 v52, s38, v52
	v_mul_f32_e32 v54, v54, v56
	v_sub_f32_e32 v52, v52, v54
	v_fma_f32 v55, v52, -0.5, v54
	v_fma_f32 v53, v52, s39, |v55|
	v_cmp_gt_f32_e64 s[42:43], v55, 0
	v_min_f32_e32 v60, v60, v53
	ds_read_b128 v[8:11], v12 offset:5120
	s_waitcnt lgkmcnt(3)
	v_sub_f32_e32 v52, v46, v44
	v_sub_f32_e32 v53, v47, v45
	v_min_f32_e32 v54, s30, v46
	v_max_f32_e32 v55, s28, v44
	v_min_f32_e32 v56, s31, v47
	v_max_f32_e32 v57, s29, v45
	v_mul_f32_e32 v52, v52, v53
	v_sub_f32_e32 v54, v54, v55
	v_sub_f32_e32 v56, v56, v57
	v_max_f32_e32 v54, 0, v54
	v_max_f32_e32 v56, 0, v56
	v_add_f32_e32 v52, s38, v52
	v_mul_f32_e32 v54, v54, v56
	v_sub_f32_e32 v52, v52, v54
	v_fma_f32 v55, v52, -0.5, v54
	v_fma_f32 v53, v52, s39, |v55|
	v_cmp_gt_f32_e64 s[44:45], v55, 0
	v_min_f32_e32 v60, v60, v53
	ds_read_b128 v[44:47], v12 offset:6144
	s_waitcnt lgkmcnt(3)
	v_sub_f32_e32 v52, v50, v48
	v_sub_f32_e32 v53, v51, v49
	v_min_f32_e32 v54, s30, v50
	v_max_f32_e32 v55, s28, v48
	v_min_f32_e32 v56, s31, v51
	v_max_f32_e32 v57, s29, v49
	v_mul_f32_e32 v52, v52, v53
	v_sub_f32_e32 v54, v54, v55
	v_sub_f32_e32 v56, v56, v57
	v_max_f32_e32 v54, 0, v54
	v_max_f32_e32 v56, 0, v56
	v_add_f32_e32 v52, s38, v52
	v_mul_f32_e32 v54, v54, v56
	v_sub_f32_e32 v52, v52, v54
	v_fma_f32 v55, v52, -0.5, v54
	v_fma_f32 v53, v52, s39, |v55|
	v_cmp_gt_f32_e64 s[46:47], v55, 0
	v_min_f32_e32 v60, v60, v53
	ds_read_b128 v[48:51], v12 offset:7168
	s_waitcnt lgkmcnt(3)
	v_sub_f32_e32 v52, v6, v4
	v_sub_f32_e32 v53, v7, v5
	v_min_f32_e32 v54, s30, v6
	v_max_f32_e32 v55, s28, v4
	v_min_f32_e32 v56, s31, v7
	v_max_f32_e32 v57, s29, v5
	v_mul_f32_e32 v52, v52, v53
	v_sub_f32_e32 v54, v54, v55
	v_sub_f32_e32 v56, v56, v57
	v_max_f32_e32 v54, 0, v54
	v_max_f32_e32 v56, 0, v56
	v_add_f32_e32 v52, s38, v52
	v_mul_f32_e32 v54, v54, v56
	v_sub_f32_e32 v52, v52, v54
	v_fma_f32 v55, v52, -0.5, v54
	v_fma_f32 v53, v52, s39, |v55|
	v_cmp_gt_f32_e64 s[48:49], v55, 0
	v_min_f32_e32 v60, v60, v53
	s_waitcnt lgkmcnt(2)
	v_sub_f32_e32 v52, v10, v8
	v_sub_f32_e32 v53, v11, v9
	v_min_f32_e32 v54, s30, v10
	v_max_f32_e32 v55, s28, v8
	v_min_f32_e32 v56, s31, v11
	v_max_f32_e32 v57, s29, v9
	v_mul_f32_e32 v52, v52, v53
	v_sub_f32_e32 v54, v54, v55
	v_sub_f32_e32 v56, v56, v57
	v_max_f32_e32 v54, 0, v54
	v_max_f32_e32 v56, 0, v56
	v_add_f32_e32 v52, s38, v52
	v_mul_f32_e32 v54, v54, v56
	v_sub_f32_e32 v52, v52, v54
	v_fma_f32 v55, v52, -0.5, v54
	v_fma_f32 v53, v52, s39, |v55|
	v_cmp_gt_f32_e64 s[50:51], v55, 0
	v_min_f32_e32 v60, v60, v53
	s_waitcnt lgkmcnt(1)
	v_sub_f32_e32 v52, v46, v44
	v_sub_f32_e32 v53, v47, v45
	v_min_f32_e32 v54, s30, v46
	v_max_f32_e32 v55, s28, v44
	v_min_f32_e32 v56, s31, v47
	v_max_f32_e32 v57, s29, v45
	v_mul_f32_e32 v52, v52, v53
	v_sub_f32_e32 v54, v54, v55
	v_sub_f32_e32 v56, v56, v57
	v_max_f32_e32 v54, 0, v54
	v_max_f32_e32 v56, 0, v56
	v_add_f32_e32 v52, s38, v52
	v_mul_f32_e32 v54, v54, v56
	v_sub_f32_e32 v52, v52, v54
	v_fma_f32 v55, v52, -0.5, v54
	v_fma_f32 v53, v52, s39, |v55|
	v_cmp_gt_f32_e64 s[52:53], v55, 0
	v_min_f32_e32 v60, v60, v53
	s_waitcnt lgkmcnt(0)
	v_sub_f32_e32 v52, v50, v48
	v_sub_f32_e32 v53, v51, v49
	v_min_f32_e32 v54, s30, v50
	v_max_f32_e32 v55, s28, v48
	v_min_f32_e32 v56, s31, v51
	v_max_f32_e32 v57, s29, v49
	v_mul_f32_e32 v52, v52, v53
	v_sub_f32_e32 v54, v54, v55
	v_sub_f32_e32 v56, v56, v57
	v_max_f32_e32 v54, 0, v54
	v_max_f32_e32 v56, 0, v56
	v_add_f32_e32 v52, s38, v52
	v_mul_f32_e32 v54, v54, v56
	v_sub_f32_e32 v52, v52, v54
	v_fma_f32 v55, v52, -0.5, v54
	v_fma_f32 v53, v52, s39, |v55|
	v_cmp_gt_f32_e64 s[54:55], v55, 0
	v_min_f32_e32 v60, v60, v53
	v_cmp_ge_f32_e32 vcc, 0, v60
	s_cbranch_vccnz .Lk1_rare

_Z22k2_resolve_rank_gatherPKfS0_PKdS0_PKiPKyPKtS0_S4_Pf:
	s_load_dwordx16 s[4:19], s[0:1], 0x0
	s_load_dwordx4 s[20:23], s[0:1], 0x40
	s_and_b32 s3, s2, 7
	s_lshr_b32 s2, s2, 3
	s_lshl_b32 s3, s3, 7
	s_add_u32 s2, s2, s3
	v_and_b32_e32 v1, 0x3ff, v0
	s_lshr_b32 s24, s2, 6
	s_and_b32 s25, s2, 63
	s_lshl_b32 s26, s24, 9
	v_lshl_add_u32 v2, v1, 1, s26
	v_lshlrev_b32_e32 v3, 4, v2
	v_lshlrev_b32_e32 v24, 2, v2
	v_lshlrev_b32_e32 v25, 3, v2
	v_mov_b32_e32 v106, 0
	v_mov_b32_e32 v107, 0
	v_mov_b32_e32 v105, 0x1800
	v_lshlrev_b32_e32 v104, 3, v1
	s_movk_i32 s30, 0x641
	s_mov_b32 s32, 0xa0b5ed8d
	s_mov_b32 s33, 0x3ed0c6f7
	s_mov_b32 s34, 0xa0b5ed8d
	s_mov_b32 s35, 0xbed0c6f7
	s_mul_i32 s31, s26, 0x1904
	v_lshrrev_b32_e32 v29, 6, v1
	s_waitcnt lgkmcnt(0)
	global_load_dwordx4 v[4:7], v3, s[16:17]
	global_load_dwordx4 v[8:11], v3, s[16:17] offset:16
	global_load_dwordx2 v[12:13], v24, s[10:11]
	global_load_dwordx2 v[16:17], v24, s[12:13]
	global_load_dwordx4 v[20:23], v25, s[8:9]
	global_load_dwordx2 v[14:15], v24, s[18:19]
	global_load_dwordx2 v[18:19], v24, s[20:21]
	s_add_u32 s28, s4, s31
	s_addc_u32 s29, s5, 0
	v_readfirstlane_b32 s27, v29
	ds_write_b64 v105, v[106:107]
	ds_write_b64 v105, v[106:107] offset:8
	ds_write_b64 v105, v[106:107] offset:16
	ds_write_b64 v104, v[106:107] offset:8448
	s_mov_b64 s[36:37], 0
	s_mov_b64 s[38:39], 0
	s_mov_b64 s[40:41], 0
	s_mov_b64 s[42:43], 0
	s_mov_b64 s[44:45], 0
	v_lshlrev_b32_e32 v2, 4, v1
	s_waitcnt vmcnt(2)
	ds_write_b128 v2, v[20:23] offset:12544
	v_lshlrev_b32_e32 v3, 5, v1
	ds_write_b128 v3, v[4:7] offset:22784
	ds_write_b128 v3, v[8:11] offset:22800
	ds_write_b64 v104, v[16:17] offset:30976
	v_and_b32_e32 v26, 0xffff, v4
	v_and_b32_e32 v27, 0xffff, v8
	v_max_u32_e32 v28, v26, v27
	v_cvt_f64_f32_e32 v[92:93], v12
	v_cvt_f64_f32_e32 v[94:95], v13
	v_add_f64 v[92:93], v[92:93], -v[20:21]
	v_add_f64 v[94:95], v[94:95], -v[22:23]
	s_waitcnt vmcnt(0)
	ds_write_b64 v104, v[14:15] offset:33024
	v_cvt_f64_f32_e32 v[96:97], v14
	v_cvt_f64_f32_e32 v[98:99], v15
	v_add_f64 v[96:97], v[96:97], -v[20:21]
	v_add_f64 v[98:99], v[98:99], -v[22:23]
	s_waitcnt lgkmcnt(0)
	s_barrier
	v_cmp_lt_u32_e32 vcc, 0, v28
	s_cbranch_vccz .Lk2_l1_done
	v_cmp_lt_u32_e32 vcc, 0, v26
	s_and_saveexec_b64 s[46:47], vcc
	s_cbranch_execz .Lk2_l1_0_0
	v_lshrrev_b32_e32 v29, 16, v4
	v_mad_u32_u24 v30, v29, s30, v16
	v_mad_u32_u24 v31, v29, s30, v18
	v_lshlrev_b32_e32 v30, 2, v30
	v_lshlrev_b32_e32 v31, 2, v31
	v_lshlrev_b32_e32 v29, 3, v29
	global_load_dword v32, v30, s[28:29]
	global_load_dword v33, v31, s[28:29]
	ds_read_b64 v[34:35], v29 offset:12544
